# v43 with priority raise for waves 4-11 (younger compute waves and loader waves) during the scan
# baseline (speedup 1.0000x reference)
_Z7k_gemm1PKfS0_PKDv4_jPKiPiS6_P15HIP_vector_typeIiLj2EEPDF16_S0_S6_S9_:
	v_lshrrev_b32_e32 v142, 6, v0
	s_mov_b32 s10, s2
	v_readfirstlane_b32 s90, v0
	s_nop 0
	s_cmp_lt_u32 s90, 0x100
	s_cbranch_scc1 .Lg1_prio_done
	s_setprio 1
